# MoE order lookups: tile-start vector read once per unit (with the unit-count word) in the GEMM unit loops and once for all nine gtok slots
# baseline (speedup 1.0000x reference)
.LBB0_40:
	v_readlane_b32 s4, v254, 35
	v_readlane_b32 s54, v253, 13
	v_readlane_b32 s55, v253, 14
	v_mov_b32_e32 v2, s4
	ds_read_b32 v2, v2
	v_lshlrev_b32_e32 v250, 2, v194
	v_add_u32_e32 v250, 0x20200, v250
	ds_read_b32 v250, v250
	s_add_i32 s85, s85, 1
	s_and_b64 vcc, exec, s[54:55]
	s_waitcnt lgkmcnt(0)
	v_readfirstlane_b32 s4, v2
	s_cbranch_vccz .LBB0_42
	s_mul_i32 s6, s85, s77
	s_mul_hi_u32 s49, s85, s76
	s_add_i32 s49, s49, s6
	s_mul_i32 s6, s85, s76
	s_add_u32 s58, s6, s44
	s_addc_u32 s59, s49, s83
	s_mov_b64 s[60:61], -1
	s_lshl_b32 s4, s4, 2
	s_cbranch_execz .LBB0_43
	s_branch .LBB0_45

.LBB0_45:
	s_mov_b64 s[54:55], 0
	s_and_b64 vcc, exec, s[60:61]
	s_cbranch_vccz .LBB0_48
	s_ashr_i32 s6, s4, 31
	v_mov_b32_e32 v2, s4
	v_mov_b32_e32 v3, s6
	v_cmp_ge_i64_e32 vcc, s[58:59], v[2:3]
	s_cbranch_vccnz .LBB0_48
	s_ashr_i32 s4, s58, 31
	s_lshr_b32 s4, s4, 30
	s_add_i32 s4, s58, s4
	s_ashr_i32 s4, s4, 2
	v_cmp_ge_i32_e32 vcc, s4, v250
	s_and_b32 s6, vcc_lo, 0xfffffffe
	s_bcnt1_i32_b32 s6, s6
	v_mov_b32_e32 v4, s6
	s_add_i32 s101, s6, 1
	v_readlane_b32 s100, v250, s6
	v_readlane_b32 s101, v250, s101
	s_waitcnt lgkmcnt(0)
	s_mov_b32 s4, s100
	s_lshl_b32 s48, s4, 2
	s_sub_i32 s48, s58, s48
	s_ashr_i32 s49, s48, 31
	s_lshr_b32 s49, s49, 27
	s_add_i32 s49, s48, s49
	s_ashr_i32 s50, s49, 5
	s_lshl_b32 s50, s50, 3
	s_mov_b32 s6, s101
	s_add_i32 s4, s50, s4
	s_sub_i32 s6, s6, s4
	s_min_i32 s6, s6, 8
	s_abs_i32 s51, s6
	v_cvt_f32_u32_e32 v2, s51
	s_sub_i32 s52, 0, s51
	s_andn2_b32 s49, s49, 31
	s_sub_i32 s49, s48, s49
	v_rcp_iflag_f32_e32 v2, v2
	s_abs_i32 s50, s49
	s_xor_b32 s48, s49, s6
	s_ashr_i32 s48, s48, 31
	v_mul_f32_e32 v2, 0x4f7ffffe, v2
	v_cvt_u32_f32_e32 v2, v2
	s_nop 0
	v_readfirstlane_b32 s53, v2
	s_mul_i32 s52, s52, s53
	s_mul_hi_u32 s52, s53, s52
	s_add_i32 s53, s53, s52
	s_mul_hi_u32 s52, s50, s53
	s_mul_i32 s53, s52, s51
	s_sub_i32 s50, s50, s53
	s_add_i32 s53, s52, 1
	s_sub_i32 s54, s50, s51
	s_cmp_ge_u32 s50, s51
	s_cselect_b32 s52, s53, s52
	s_cselect_b32 s50, s54, s50
	s_add_i32 s53, s52, 1
	s_cmp_ge_u32 s50, s51
	s_cselect_b32 s50, s53, s52
	s_xor_b32 s50, s50, s48
	s_sub_i32 s48, s50, s48
	s_mul_i32 s6, s48, s6
	s_sub_i32 s6, s49, s6
	s_add_i32 s50, s4, s6
	v_readfirstlane_b32 s52, v4
	s_mov_b64 s[54:55], -1

.LBB0_141:
	s_ashr_i32 s41, s40, 31
	s_mov_b64 s[36:37], 0
	s_and_b64 vcc, exec, s[38:39]
	s_mov_b32 s78, s80
	s_mov_b32 s48, s7
	s_cbranch_vccz .LBB0_144
	s_waitcnt vmcnt(0)
	v_mov_b64_e32 v[2:3], s[40:41]
	v_cmp_ge_i64_e32 vcc, s[26:27], v[2:3]
	s_mov_b32 s48, s7
	s_mov_b32 s78, s80
	s_cbranch_vccnz .LBB0_144
	s_ashr_i32 s4, s26, 31
	s_lshr_b32 s4, s4, 29
	s_add_i32 s4, s26, s4
	s_ashr_i32 s4, s4, 3
	s_mov_b64 s[36:37], -1
	v_lshlrev_b32_e32 v160, 2, v194
	v_add_u32_e32 v160, 0x20200, v160
	ds_read_b32 v160, v160
	s_waitcnt lgkmcnt(0)
	v_cmp_ge_i32_e32 vcc, s4, v160
	s_and_b32 s5, vcc_lo, 0xfffffffe
	s_bcnt1_i32_b32 s5, s5
	v_mov_b32_e32 v0, s5
	s_add_i32 s101, s5, 1
	v_readlane_b32 s100, v160, s5
	v_readlane_b32 s101, v160, s101
	v_readfirstlane_b32 s48, v0
	s_waitcnt lgkmcnt(0)
	s_mov_b32 s4, s100
	s_lshl_b32 s6, s4, 3
	s_sub_i32 s6, s26, s6
	s_ashr_i32 s14, s6, 31
	s_lshr_b32 s14, s14, 27
	s_add_i32 s14, s6, s14
	s_ashr_i32 s15, s14, 5
	s_lshl_b32 s15, s15, 2
	s_mov_b32 s5, s101
	s_add_i32 s4, s15, s4
	s_sub_i32 s5, s5, s4
	s_min_i32 s5, s5, 4
	s_andn2_b32 s14, s14, 31
	s_sub_i32 s6, s6, s14
	s_lshr_b32 s100, s5, 1
	s_lshr_b32 s100, s6, s100
	s_mul_i32 s101, s6, 22
	s_lshr_b32 s101, s101, 6
	s_cmp_eq_u32 s5, 3
	s_cselect_b32 s100, s101, s100
	s_mul_i32 s101, s100, s5
	s_sub_i32 s101, s6, s101
	s_add_i32 s78, s4, s101

.LBB0_151:
	s_mov_b64 s[36:37], 0
	s_and_b64 vcc, exec, s[50:51]
	s_cbranch_vccz .LBB0_154
	v_mov_b64_e32 v[4:5], s[40:41]
	v_cmp_ge_i64_e32 vcc, s[26:27], v[4:5]
	s_cbranch_vccnz .LBB0_154
	s_ashr_i32 s4, s26, 31
	s_lshr_b32 s4, s4, 29
	s_add_i32 s4, s26, s4
	s_ashr_i32 s4, s4, 3
	s_mov_b64 s[36:37], -1
	s_waitcnt vmcnt(14)
	v_cmp_ge_i32_e32 vcc, s4, v160
	s_and_b32 s6, vcc_lo, 0xfffffffe
	s_bcnt1_i32_b32 s6, s6
	v_mov_b32_e32 v3, s6
	s_add_i32 s101, s6, 1
	v_readlane_b32 s100, v160, s6
	v_readlane_b32 s101, v160, s101
	v_readfirstlane_b32 s48, v3
	s_waitcnt lgkmcnt(0)
	s_mov_b32 s4, s100
	s_lshl_b32 s14, s4, 3
	s_sub_i32 s14, s26, s14
	s_ashr_i32 s15, s14, 31
	s_lshr_b32 s15, s15, 27
	s_add_i32 s15, s14, s15
	s_ashr_i32 s16, s15, 5
	s_lshl_b32 s16, s16, 2
	s_mov_b32 s6, s101
	s_add_i32 s4, s16, s4
	s_sub_i32 s6, s6, s4
	s_min_i32 s6, s6, 4
	s_andn2_b32 s15, s15, 31
	s_sub_i32 s14, s14, s15
	s_lshr_b32 s100, s6, 1
	s_lshr_b32 s100, s14, s100
	s_mul_i32 s101, s14, 22
	s_lshr_b32 s101, s101, 6
	s_cmp_eq_u32 s6, 3
	s_cselect_b32 s100, s101, s100
	s_mul_i32 s101, s100, s6
	s_sub_i32 s101, s14, s101
	s_add_i32 s78, s4, s101

.LBB0_161:
	s_mov_b64 s[36:37], 0
	s_and_b64 vcc, exec, s[50:51]
	s_cbranch_vccz .LBB0_164
	v_mov_b64_e32 v[4:5], s[40:41]
	v_cmp_ge_i64_e32 vcc, s[26:27], v[4:5]
	s_cbranch_vccnz .LBB0_164
	s_ashr_i32 s4, s26, 31
	s_lshr_b32 s4, s4, 29
	s_add_i32 s4, s26, s4
	s_ashr_i32 s4, s4, 3
	s_mov_b64 s[36:37], -1
	s_waitcnt vmcnt(14)
	v_cmp_ge_i32_e32 vcc, s4, v160
	s_and_b32 s6, vcc_lo, 0xfffffffe
	s_bcnt1_i32_b32 s6, s6
	v_mov_b32_e32 v6, s6
	s_add_i32 s101, s6, 1
	v_readlane_b32 s100, v160, s6
	v_readlane_b32 s101, v160, s101
	v_readfirstlane_b32 s48, v6
	s_waitcnt lgkmcnt(0)
	s_mov_b32 s4, s100
	s_lshl_b32 s14, s4, 3
	s_sub_i32 s14, s26, s14
	s_ashr_i32 s15, s14, 31
	s_lshr_b32 s15, s15, 27
	s_add_i32 s15, s14, s15
	s_ashr_i32 s16, s15, 5
	s_lshl_b32 s16, s16, 2
	s_mov_b32 s6, s101
	s_add_i32 s4, s16, s4
	s_sub_i32 s6, s6, s4
	s_min_i32 s6, s6, 4
	s_andn2_b32 s15, s15, 31
	s_sub_i32 s14, s14, s15
	s_lshr_b32 s100, s6, 1
	s_lshr_b32 s100, s14, s100
	s_mul_i32 s101, s14, 22
	s_lshr_b32 s101, s101, 6
	s_cmp_eq_u32 s6, 3
	s_cselect_b32 s100, s101, s100
	s_mul_i32 s101, s100, s6
	s_sub_i32 s101, s14, s101
	s_add_i32 s78, s4, s101

.LBB0_171:
	s_mov_b64 s[36:37], 0
	s_and_b64 vcc, exec, s[50:51]
	s_cbranch_vccz .LBB0_174
	s_waitcnt vmcnt(14)
	v_mov_b64_e32 v[6:7], s[40:41]
	v_cmp_ge_i64_e32 vcc, s[26:27], v[6:7]
	s_cbranch_vccnz .LBB0_174
	s_ashr_i32 s4, s26, 31
	s_lshr_b32 s4, s4, 29
	s_add_i32 s4, s26, s4
	s_ashr_i32 s4, s4, 3
	s_mov_b64 s[36:37], -1
	v_cmp_ge_i32_e32 vcc, s4, v160
	s_and_b32 s6, vcc_lo, 0xfffffffe
	s_bcnt1_i32_b32 s6, s6
	v_mov_b32_e32 v5, s6
	s_add_i32 s101, s6, 1
	v_readlane_b32 s100, v160, s6
	v_readlane_b32 s101, v160, s101
	v_readfirstlane_b32 s48, v5
	s_waitcnt lgkmcnt(0)
	s_mov_b32 s4, s100
	s_lshl_b32 s14, s4, 3
	s_sub_i32 s14, s26, s14
	s_ashr_i32 s15, s14, 31
	s_lshr_b32 s15, s15, 27
	s_add_i32 s15, s14, s15
	s_ashr_i32 s16, s15, 5
	s_lshl_b32 s16, s16, 2
	s_mov_b32 s6, s101
	s_add_i32 s4, s16, s4
	s_sub_i32 s6, s6, s4
	s_min_i32 s6, s6, 4
	s_andn2_b32 s15, s15, 31
	s_sub_i32 s14, s14, s15
	s_lshr_b32 s100, s6, 1
	s_lshr_b32 s100, s14, s100
	s_mul_i32 s101, s14, 22
	s_lshr_b32 s101, s101, 6
	s_cmp_eq_u32 s6, 3
	s_cselect_b32 s100, s101, s100
	s_mul_i32 s101, s100, s6
	s_sub_i32 s101, s14, s101
	s_add_i32 s78, s4, s101

.LBB0_181:
	s_mov_b64 s[36:37], 0
	s_and_b64 vcc, exec, s[50:51]
	s_cbranch_vccz .LBB0_184
	s_waitcnt vmcnt(14)
	v_mov_b64_e32 v[6:7], s[40:41]
	v_cmp_ge_i64_e32 vcc, s[26:27], v[6:7]
	s_cbranch_vccnz .LBB0_184
	s_ashr_i32 s4, s26, 31
	s_lshr_b32 s4, s4, 29
	s_add_i32 s4, s26, s4
	s_ashr_i32 s4, s4, 3
	s_mov_b64 s[36:37], -1
	v_cmp_ge_i32_e32 vcc, s4, v160
	s_and_b32 s6, vcc_lo, 0xfffffffe
	s_bcnt1_i32_b32 s6, s6
	v_mov_b32_e32 v8, s6
	s_add_i32 s101, s6, 1
	v_readlane_b32 s100, v160, s6
	v_readlane_b32 s101, v160, s101
	v_readfirstlane_b32 s48, v8
	s_waitcnt lgkmcnt(0)
	s_mov_b32 s4, s100
	s_lshl_b32 s14, s4, 3
	s_sub_i32 s14, s26, s14
	s_ashr_i32 s15, s14, 31
	s_lshr_b32 s15, s15, 27
	s_add_i32 s15, s14, s15
	s_ashr_i32 s16, s15, 5
	s_lshl_b32 s16, s16, 2
	s_mov_b32 s6, s101
	s_add_i32 s4, s16, s4
	s_sub_i32 s6, s6, s4
	s_min_i32 s6, s6, 4
	s_andn2_b32 s15, s15, 31
	s_sub_i32 s14, s14, s15
	s_lshr_b32 s100, s6, 1
	s_lshr_b32 s100, s14, s100
	s_mul_i32 s101, s14, 22
	s_lshr_b32 s101, s101, 6
	s_cmp_eq_u32 s6, 3
	s_cselect_b32 s100, s101, s100
	s_mul_i32 s101, s100, s6
	s_sub_i32 s101, s14, s101
	s_add_i32 s78, s4, s101

.LBB0_191:
	s_mov_b64 s[36:37], 0
	s_and_b64 vcc, exec, s[50:51]
	s_cbranch_vccz .LBB0_194
	v_mov_b64_e32 v[8:9], s[40:41]
	v_cmp_ge_i64_e32 vcc, s[26:27], v[8:9]
	s_cbranch_vccnz .LBB0_194
	s_ashr_i32 s4, s26, 31
	s_lshr_b32 s4, s4, 29
	s_add_i32 s4, s26, s4
	s_ashr_i32 s4, s4, 3
	s_mov_b64 s[36:37], -1
	s_waitcnt vmcnt(13)
	v_cmp_ge_i32_e32 vcc, s4, v160
	s_and_b32 s6, vcc_lo, 0xfffffffe
	s_bcnt1_i32_b32 s6, s6
	v_mov_b32_e32 v7, s6
	s_add_i32 s101, s6, 1
	v_readlane_b32 s100, v160, s6
	v_readlane_b32 s101, v160, s101
	v_readfirstlane_b32 s48, v7
	s_waitcnt lgkmcnt(0)
	s_mov_b32 s4, s100
	s_lshl_b32 s14, s4, 3
	s_sub_i32 s14, s26, s14
	s_ashr_i32 s15, s14, 31
	s_lshr_b32 s15, s15, 27
	s_add_i32 s15, s14, s15
	s_ashr_i32 s16, s15, 5
	s_lshl_b32 s16, s16, 2
	s_mov_b32 s6, s101
	s_add_i32 s4, s16, s4
	s_sub_i32 s6, s6, s4
	s_min_i32 s6, s6, 4
	s_andn2_b32 s15, s15, 31
	s_sub_i32 s14, s14, s15
	s_lshr_b32 s100, s6, 1
	s_lshr_b32 s100, s14, s100
	s_mul_i32 s101, s14, 22
	s_lshr_b32 s101, s101, 6
	s_cmp_eq_u32 s6, 3
	s_cselect_b32 s100, s101, s100
	s_mul_i32 s101, s100, s6
	s_sub_i32 s101, s14, s101
	s_add_i32 s78, s4, s101

.LBB0_201:
	s_mov_b64 s[36:37], 0
	s_and_b64 vcc, exec, s[50:51]
	s_cbranch_vccz .LBB0_204
	v_mov_b64_e32 v[8:9], s[40:41]
	v_cmp_ge_i64_e32 vcc, s[26:27], v[8:9]
	s_cbranch_vccnz .LBB0_204
	s_ashr_i32 s4, s26, 31
	s_lshr_b32 s4, s4, 29
	s_add_i32 s4, s26, s4
	s_ashr_i32 s4, s4, 3
	s_mov_b64 s[36:37], -1
	s_waitcnt vmcnt(13)
	v_cmp_ge_i32_e32 vcc, s4, v160
	s_and_b32 s6, vcc_lo, 0xfffffffe
	s_bcnt1_i32_b32 s6, s6
	v_mov_b32_e32 v10, s6
	s_add_i32 s101, s6, 1
	v_readlane_b32 s100, v160, s6
	v_readlane_b32 s101, v160, s101
	v_readfirstlane_b32 s48, v10
	s_waitcnt lgkmcnt(0)
	s_mov_b32 s4, s100
	s_lshl_b32 s14, s4, 3
	s_sub_i32 s14, s26, s14
	s_ashr_i32 s15, s14, 31
	s_lshr_b32 s15, s15, 27
	s_add_i32 s15, s14, s15
	s_ashr_i32 s16, s15, 5
	s_lshl_b32 s16, s16, 2
	s_mov_b32 s6, s101
	s_add_i32 s4, s16, s4
	s_sub_i32 s6, s6, s4
	s_min_i32 s6, s6, 4
	s_andn2_b32 s15, s15, 31
	s_sub_i32 s14, s14, s15
	s_lshr_b32 s100, s6, 1
	s_lshr_b32 s100, s14, s100
	s_mul_i32 s101, s14, 22
	s_lshr_b32 s101, s101, 6
	s_cmp_eq_u32 s6, 3
	s_cselect_b32 s100, s101, s100
	s_mul_i32 s101, s100, s6
	s_sub_i32 s101, s14, s101
	s_add_i32 s78, s4, s101

.LBB0_211:
	s_mov_b64 s[36:37], 0
	s_and_b64 vcc, exec, s[50:51]
	s_cbranch_vccz .LBB0_214
	s_waitcnt vmcnt(13)
	v_mov_b64_e32 v[10:11], s[40:41]
	v_cmp_ge_i64_e32 vcc, s[26:27], v[10:11]
	s_cbranch_vccnz .LBB0_214
	s_ashr_i32 s4, s26, 31
	s_lshr_b32 s4, s4, 29
	s_add_i32 s4, s26, s4
	s_ashr_i32 s4, s4, 3
	s_mov_b64 s[36:37], -1
	v_cmp_ge_i32_e32 vcc, s4, v160
	s_and_b32 s6, vcc_lo, 0xfffffffe
	s_bcnt1_i32_b32 s6, s6
	v_mov_b32_e32 v9, s6
	s_add_i32 s101, s6, 1
	v_readlane_b32 s100, v160, s6
	v_readlane_b32 s101, v160, s101
	v_readfirstlane_b32 s48, v9
	s_waitcnt lgkmcnt(0)
	s_mov_b32 s4, s100
	s_lshl_b32 s14, s4, 3
	s_sub_i32 s14, s26, s14
	s_ashr_i32 s15, s14, 31
	s_lshr_b32 s15, s15, 27
	s_add_i32 s15, s14, s15
	s_ashr_i32 s16, s15, 5
	s_lshl_b32 s16, s16, 2
	s_mov_b32 s6, s101
	s_add_i32 s4, s16, s4
	s_sub_i32 s6, s6, s4
	s_min_i32 s6, s6, 4
	s_andn2_b32 s15, s15, 31
	s_sub_i32 s14, s14, s15
	s_lshr_b32 s100, s6, 1
	s_lshr_b32 s100, s14, s100
	s_mul_i32 s101, s14, 22
	s_lshr_b32 s101, s101, 6
	s_cmp_eq_u32 s6, 3
	s_cselect_b32 s100, s101, s100
	s_mul_i32 s101, s100, s6
	s_sub_i32 s101, s14, s101
	s_add_i32 s78, s4, s101

.LBB0_221:
	s_mov_b64 s[36:37], 0
	s_and_b64 vcc, exec, s[38:39]
	s_cbranch_vccz .LBB0_224
	s_waitcnt vmcnt(13)
	v_mov_b64_e32 v[10:11], s[40:41]
	v_cmp_ge_i64_e32 vcc, s[26:27], v[10:11]
	s_cbranch_vccnz .LBB0_224
	s_ashr_i32 s4, s26, 31
	s_lshr_b32 s4, s4, 29
	s_add_i32 s4, s26, s4
	s_ashr_i32 s4, s4, 3
	s_mov_b64 s[36:37], -1
	v_cmp_ge_i32_e32 vcc, s4, v160
	s_and_b32 s6, vcc_lo, 0xfffffffe
	s_bcnt1_i32_b32 s6, s6
	v_mov_b32_e32 v12, s6
	s_add_i32 s101, s6, 1
	v_readlane_b32 s100, v160, s6
	v_readlane_b32 s101, v160, s101
	v_readfirstlane_b32 s48, v12
	s_waitcnt lgkmcnt(0)
	s_mov_b32 s4, s100
	s_lshl_b32 s14, s4, 3
	s_sub_i32 s14, s26, s14
	s_ashr_i32 s15, s14, 31
	s_lshr_b32 s15, s15, 27
	s_add_i32 s15, s14, s15
	s_ashr_i32 s16, s15, 5
	s_lshl_b32 s16, s16, 2
	s_mov_b32 s6, s101
	s_add_i32 s4, s16, s4
	s_sub_i32 s6, s6, s4
	s_min_i32 s6, s6, 4
	s_andn2_b32 s15, s15, 31
	s_sub_i32 s14, s14, s15
	s_lshr_b32 s100, s6, 1
	s_lshr_b32 s100, s14, s100
	s_mul_i32 s101, s14, 22
	s_lshr_b32 s101, s101, 6
	s_cmp_eq_u32 s6, 3
	s_cselect_b32 s100, s101, s100
	s_mul_i32 s101, s100, s6
	s_sub_i32 s101, s14, s101
	s_add_i32 s78, s4, s101

.LBB0_231:
	v_lshlrev_b32_e32 v188, 4, v192
	v_and_b32_e32 v189, 15, v194
	s_and_b64 vcc, exec, s[38:39]
	s_cbranch_vccz .LBB0_257
	s_ashr_i32 s5, s4, 31
	v_mov_b32_e32 v2, s4
	v_mov_b32_e32 v3, s5
	v_cmp_ge_i64_e32 vcc, s[26:27], v[2:3]
	s_cbranch_vccnz .LBB0_257
	v_ashrrev_i32_e32 v0, 31, v192
	v_lshrrev_b32_e32 v0, 26, v0
	v_add_u32_e32 v0, v192, v0
	v_ashrrev_i32_e32 v3, 6, v0
	v_ashrrev_i32_e32 v0, 31, v188
	v_lshrrev_b32_e32 v0, 22, v0
	v_add_u32_e32 v0, v188, v0
	v_and_b32_e32 v0, 0xfffffc00, v0
	v_sub_u32_e32 v2, v188, v0
	v_lshrrev_b32_e32 v0, 4, v2
	v_bitop3_b32 v4, v0, v2, 32 bitop3:0x6c
	v_ashrrev_i32_e32 v2, 31, v2
	v_lshrrev_b32_e32 v2, 26, v2
	v_add_u32_e32 v5, v4, v2
	v_ashrrev_i32_e32 v2, 6, v5
	v_and_b32_e32 v5, 0xc0, v5
	v_sub_u32_e32 v4, v4, v5
	s_add_u32 s40, s46, 0x2e000000
	v_lshlrev_b32_e32 v0, 3, v3
	v_lshlrev_b32_e32 v3, 5, v3
	v_ashrrev_i16_sdwa v4, v225, sext(v4) dst_sel:DWORD dst_unused:UNUSED_PAD src0_sel:DWORD src1_sel:BYTE_0
	s_addc_u32 s41, s47, 0
	s_ashr_i32 s83, s82, 31
	v_and_b32_e32 v0, -16, v0
	v_and_b32_e32 v3, 32, v3
	v_bfe_i32 v4, v4, 0, 16
	v_writelane_b32 v255, s82, 10
	s_lshl_b64 s[4:5], s[82:83], 26
	v_add_u32_e32 v6, v2, v0
	v_add_lshl_u32 v193, v3, v4, 1
	v_add_u32_e32 v3, 0x2000, v188
	v_writelane_b32 v255, s83, 11
	s_add_u32 s82, s49, s4
	v_lshlrev_b32_e32 v5, 1, v6
	v_lshrrev_b32_e32 v7, 2, v6
	v_and_b32_e32 v8, 3, v2
	s_mov_b32 s4, 0x3fffe0
	v_ashrrev_i32_e32 v4, 31, v3
	v_and_b32_e32 v5, 24, v5
	v_and_b32_e32 v7, 4, v7
	v_and_or_b32 v6, v6, s4, v8
	v_lshrrev_b32_e32 v4, 22, v4
	v_or3_b32 v5, v6, v7, v5
	v_add_u32_e32 v4, v3, v4
	v_lshl_add_u32 v162, v5, 10, v193
	v_ashrrev_i32_e32 v5, 10, v4
	v_mul_i32_i24_e32 v4, 0x400, v5
	v_sub_u32_e32 v3, v3, v4
	v_lshrrev_b32_e32 v4, 4, v3
	v_bitop3_b32 v6, v4, v3, 32 bitop3:0x6c
	v_ashrrev_i32_e32 v4, 31, v6
	v_lshrrev_b32_e32 v4, 26, v4
	v_lshlrev_b32_e32 v3, 3, v5
	v_add_u32_e32 v7, v6, v4
	v_and_b32_e32 v3, -16, v3
	v_ashrrev_i32_e32 v4, 6, v7
	v_and_b32_e32 v7, 0xc0, v7
	v_add_u32_e32 v8, v4, v3
	v_sub_u32_e32 v6, v6, v7
	v_lshlrev_b32_e32 v5, 5, v5
	v_ashrrev_i16_sdwa v6, v225, sext(v6) dst_sel:DWORD dst_unused:UNUSED_PAD src0_sel:DWORD src1_sel:BYTE_0
	v_lshlrev_b32_e32 v7, 1, v8
	v_lshrrev_b32_e32 v9, 2, v8
	v_and_b32_e32 v10, 3, v4
	s_addc_u32 s83, s73, s5
	v_and_b32_e32 v5, 32, v5
	v_bfe_i32 v6, v6, 0, 16
	v_and_b32_e32 v7, 24, v7
	v_and_b32_e32 v9, 4, v9
	v_and_or_b32 v8, v8, s4, v10
	v_or3_b32 v7, v8, v9, v7
	v_add_lshl_u32 v195, v5, v6, 1
	v_lshl_add_u32 v164, v7, 10, v195
	s_ashr_i32 s4, s26, 31
	s_lshr_b32 s4, s4, 29
	s_add_i32 s4, s26, s4
	s_ashr_i32 s4, s4, 3
	s_ashr_i32 s16, s6, 6
	s_ashr_i32 s15, s6, 8
	s_lshl_b32 s92, s16, 10
	v_lshlrev_b32_e32 v196, 2, v2
	v_lshlrev_b32_e32 v197, 2, v0
	v_lshlrev_b32_e32 v198, 2, v4
	v_lshlrev_b32_e32 v199, 2, v3
	v_mov_b32_e32 v163, v1
	v_mov_b32_e32 v165, v1
	v_cmp_ge_i32_e32 vcc, s4, v160
	s_and_b32 s5, vcc_lo, 0xfffffffe
	s_bcnt1_i32_b32 s5, s5
	v_mov_b32_e32 v5, s5
	s_add_i32 s101, s5, 1
	v_readlane_b32 s100, v160, s5
	v_readlane_b32 s101, v160, s101
	v_readfirstlane_b32 s68, v5
	s_waitcnt lgkmcnt(0)
	s_mov_b32 s4, s100
	s_lshl_b32 s14, s4, 3
	s_sub_i32 s14, s26, s14
	s_ashr_i32 s17, s14, 31
	s_lshr_b32 s17, s17, 27
	s_add_i32 s17, s14, s17
	s_ashr_i32 s26, s17, 5
	s_lshl_b32 s26, s26, 2
	s_mov_b32 s5, s101
	s_add_i32 s4, s26, s4
	s_sub_i32 s5, s5, s4
	s_min_i32 s5, s5, 4
	s_andn2_b32 s17, s17, 31
	s_sub_i32 s14, s14, s17
	s_lshr_b32 s100, s5, 1
	s_lshr_b32 s100, s14, s100
	s_mul_i32 s101, s14, 22
	s_lshr_b32 s101, s101, 6
	s_cmp_eq_u32 s5, 3
	s_cselect_b32 s100, s101, s100
	s_mul_i32 s101, s100, s5
	s_sub_i32 s5, s14, s101
	s_mov_b32 s66, s100
	s_add_i32 s14, 0, 0x21000
	v_add3_u32 v0, s14, v196, v197
	ds_read_b32 v0, v0
	s_ashr_i32 s69, s68, 31
	s_ashr_i32 s67, s66, 31
	s_add_i32 s75, s4, s5
	s_lshl_b64 s[4:5], s[68:69], 21
	s_waitcnt lgkmcnt(0)
	v_lshl_add_u32 v168, v0, 10, v193
	v_add3_u32 v0, s14, v198, v199
	ds_read_b32 v0, v0
	v_readlane_b32 s14, v254, 52
	s_lshl_b64 s[26:27], s[66:67], 18
	s_add_u32 s4, s82, s4
	s_addc_u32 s5, s83, s5
	s_waitcnt lgkmcnt(0)
	v_lshl_add_u32 v170, v0, 10, v195
	v_add3_u32 v0, s14, v196, v197
	ds_read_b32 v0, v0
	s_add_u32 s26, s4, s26
	s_addc_u32 s27, s5, s27
	s_add_i32 s93, s92, 0
	s_add_i32 m0, s93, 0x10000
	s_waitcnt lgkmcnt(0)
	v_lshl_add_u32 v172, v0, 10, v193
	v_add3_u32 v0, s14, v198, v199
	ds_read_b32 v0, v0
	global_load_lds_dwordx4 v162, s[26:27]
	s_add_i32 m0, s93, 0x12000
	s_add_u32 s4, s26, 0x20000
	global_load_lds_dwordx4 v164, s[26:27]
	s_addc_u32 s5, s27, 0
	s_add_i32 m0, s93, 0x14000
	s_add_i32 s79, s93, 0x2000
	global_load_lds_dwordx4 v162, s[4:5]
	s_add_i32 m0, s93, 0x16000
	s_add_i32 s84, s93, 0x4000
	global_load_lds_dwordx4 v164, s[4:5]
	s_mov_b32 m0, s93
	s_add_i32 s85, s93, 0x6000
	global_load_lds_dwordx4 v168, s[40:41]
	s_mov_b32 m0, s79
	s_waitcnt lgkmcnt(0)
	v_lshl_add_u32 v174, v0, 10, v195
	global_load_lds_dwordx4 v170, s[40:41]
	s_mov_b32 m0, s84
	s_cmp_eq_u32 s15, 1
	global_load_lds_dwordx4 v172, s[40:41]
	s_mov_b32 m0, s85
	v_lshl_add_u64 v[2:3], s[26:27], 0, v[162:163]
	global_load_lds_dwordx4 v174, s[40:41]
	v_lshl_add_u64 v[4:5], s[26:27], 0, v[164:165]
	s_cselect_b64 s[42:43], -1, 0
	s_cmp_lg_u32 s15, 1
	s_cbranch_scc1 .LBB0_235
	s_barrier

.LBB0_238:
	v_readlane_b32 s4, v254, 35
	v_readlane_b32 s36, v253, 13
	v_readlane_b32 s37, v253, 14
	v_mov_b32_e32 v0, s4
	ds_read_b32 v0, v0
	v_lshlrev_b32_e32 v250, 2, v194
	v_add_u32_e32 v250, 0x20200, v250
	ds_read_b32 v250, v250
	s_add_i32 s17, s17, 1
	s_and_b64 vcc, exec, s[36:37]
	s_waitcnt lgkmcnt(0)
	v_readfirstlane_b32 s4, v0
	s_cbranch_vccz .LBB0_240
	s_mul_i32 s6, s17, s77
	s_mul_hi_u32 s31, s17, s76
	s_add_i32 s31, s31, s6
	s_mul_i32 s6, s17, s76
	s_add_u32 s36, s6, s44
	s_addc_u32 s37, s31, s45
	s_mov_b64 s[38:39], -1
	s_lshl_b32 s4, s4, 3
	s_cbranch_execz .LBB0_241
	s_branch .LBB0_243

.LBB0_243:
	s_mov_b64 s[70:71], 0
	s_and_b64 vcc, exec, s[38:39]
	s_cbranch_vccz .LBB0_246
	s_ashr_i32 s6, s4, 31
	v_mov_b32_e32 v2, s4
	v_mov_b32_e32 v3, s6
	v_cmp_ge_i64_e32 vcc, s[36:37], v[2:3]
	s_cbranch_vccnz .LBB0_246
	s_ashr_i32 s4, s36, 31
	s_lshr_b32 s4, s4, 29
	s_add_i32 s4, s36, s4
	s_ashr_i32 s4, s4, 3
	s_mov_b64 s[70:71], -1
	v_cmp_ge_i32_e32 vcc, s4, v250
	s_and_b32 s6, vcc_lo, 0xfffffffe
	s_bcnt1_i32_b32 s6, s6
	v_mov_b32_e32 v0, s6
	s_add_i32 s101, s6, 1
	v_readlane_b32 s100, v250, s6
	v_readlane_b32 s101, v250, s101
	v_readfirstlane_b32 s62, v0
	s_waitcnt lgkmcnt(0)
	s_mov_b32 s4, s100
	s_lshl_b32 s30, s4, 3
	s_sub_i32 s30, s36, s30
	s_ashr_i32 s31, s30, 31
	s_lshr_b32 s31, s31, 27
	s_add_i32 s31, s30, s31
	s_ashr_i32 s36, s31, 5
	s_lshl_b32 s36, s36, 2
	s_mov_b32 s6, s101
	s_add_i32 s4, s36, s4
	s_sub_i32 s6, s6, s4
	s_min_i32 s6, s6, 4
	s_andn2_b32 s31, s31, 31
	s_sub_i32 s30, s30, s31
	s_lshr_b32 s100, s6, 1
	s_lshr_b32 s100, s30, s100
	s_mul_i32 s101, s30, 22
	s_lshr_b32 s101, s101, 6
	s_cmp_eq_u32 s6, 3
	s_cselect_b32 s100, s101, s100
	s_mul_i32 s101, s100, s6
	s_sub_i32 s6, s30, s101
	s_mov_b32 s60, s100
	s_add_i32 s30, s4, s6
